# final combine+norm loop: gain vector loaded once before the row loop
# baseline (speedup 1.0000x reference)
; __global__ void __launch_bounds__(NWAVES * 64, 2) trunk_fwd(Args args) {
;     ...
;                 for (int m = gw; m < M; m += ngw) {
;                     const int p0 = TOKP[2 * m], p1 = TOKP[2 * m + 1]; const float g0 = TOKW[2 * m], g1 = TOKW[2 * m + 1];
;                     const f32x4* xr = (const f32x4*)(XA + (size_t)m * D) + lane; const v2u* y0 = (const v2u*)(YPERM + (size_t)p0 * D) + lane; const v2u* y1 = (const v2u*)(YPERM + (size_t)p1 * D) + lane;
;                     const v2u* z0 = (const v2u*)(HPERM + (size_t)p0 * D) + lane; const v2u* z1 = (const v2u*)(HPERM + (size_t)p1 * D) + lane;
;                     f32x4 v[8]; float s = 0.f;
; #pragma unroll
;                     for (int jj = 0; jj < 8; ++jj) { const v2u a = y0[64 * jj], c = y1[64 * jj], a2 = z0[64 * jj], c2 = z1[64 * jj]; f32x4 x = xr[64 * jj];
;                         x.x += g0 * (bflo(a.x) + bflo(a2.x)) + g1 * (bflo(c.x) + bflo(c2.x)); x.y += g0 * (bfhi(a.x) + bfhi(a2.x)) + g1 * (bfhi(c.x) + bfhi(c2.x));
;                         x.z += g0 * (bflo(a.y) + bflo(a2.y)) + g1 * (bflo(c.y) + bflo(c2.y)); x.w += g0 * (bfhi(a.y) + bfhi(a2.y)) + g1 * (bfhi(c.y) + bfhi(c2.y));
;                         v[jj] = x; s += (x.x * x.x + x.y * x.y) + (x.z * x.z + x.w * x.w); }
;                     const float rstd = 1.0f / sqrtf(wave_sum(s) * (1.0f / D) + EPS);
;                     const f32x4* gr = (const f32x4*)args.in[I_NF] + lane; f32x4* orow = (f32x4*)(args.out + (size_t)m * D) + lane;
.LBB0_1346:
	v_mov_b32_e32 v2, v0
	s_mov_b64 s[4:5], -1
	v_readfirstlane_b32 s0, v2
	s_ashr_i32 s10, s0, 6
	v_readlane_b32 s0, v250, 5
	s_add_i32 s6, s10, s0
	s_cmpk_lt_i32 s6, 0x2000
	s_cselect_b64 s[0:1], -1, 0
	v_and_b32_e32 v1, 63, v2
	v_cndmask_b32_e64 v2, 0, 1, s[0:1]
	s_and_b64 vcc, exec, s[38:39]
	v_cmp_ne_u32_e64 s[0:1], 1, v2
	s_cbranch_vccnz .LBB0_1351
	v_readlane_b32 s16, v254, 59
	v_readlane_b32 s17, v254, 60
	v_readlane_b32 s18, v252, 29
	v_readlane_b32 s38, v254, 61
	s_and_b64 vcc, exec, s[0:1]
	v_readlane_b32 s17, v252, 17
	v_readlane_b32 s19, v252, 30
	s_movk_i32 s20, 0x1000
	v_readlane_b32 s21, v254, 43
	s_mov_b32 s22, 0xf800000
	s_mov_b32 s28, 0x36da2000
	v_readlane_b32 s39, v254, 62
	s_cbranch_vccnz .LBB0_1350
	v_and_b32_e32 v2, 64, v228
	v_add_u32_e32 v2, 64, v2
	v_xor_b32_e32 v3, 1, v228
	v_cmp_lt_i32_e32 vcc, v3, v2
	v_readlane_b32 s4, v252, 47
	v_lshlrev_b32_e32 v186, 3, v1
	v_cndmask_b32_e32 v3, v228, v3, vcc
	v_lshlrev_b32_e32 v73, 2, v3
	v_xor_b32_e32 v3, 2, v228
	v_cmp_lt_i32_e32 vcc, v3, v2
	v_readlane_b32 s5, v252, 48
	v_readlane_b32 s12, v255, 3
	v_cndmask_b32_e32 v3, v228, v3, vcc
	v_lshl_add_u64 v[28:29], s[4:5], 0, v[186:187]
	v_readlane_b32 s4, v252, 31
	v_lshlrev_b32_e32 v75, 2, v3
	v_xor_b32_e32 v3, 4, v228
	v_readlane_b32 s5, v252, 32
	v_cmp_lt_i32_e32 vcc, v3, v2
	v_readlane_b32 s14, v255, 5
	v_lshl_add_u64 v[30:31], s[4:5], 0, v[186:187]
	v_cndmask_b32_e32 v3, v228, v3, vcc
	v_lshlrev_b32_e32 v186, 4, v1
	v_readlane_b32 s15, v255, 6
	v_lshlrev_b32_e32 v108, 2, v3
	v_xor_b32_e32 v3, 8, v228
	v_lshl_add_u64 v[32:33], s[14:15], 0, v[186:187]
	s_mov_b64 s[4:5], 0x1000
	v_cmp_lt_i32_e32 vcc, v3, v2
	v_lshl_add_u64 v[34:35], v[32:33], 0, s[4:5]
	s_mov_b64 s[4:5], 0x1400
	v_cndmask_b32_e32 v3, v228, v3, vcc
	v_lshl_add_u64 v[36:37], v[32:33], 0, s[4:5]
	s_mov_b64 s[4:5], 0x1800
	v_lshlrev_b32_e32 v109, 2, v3
	v_xor_b32_e32 v3, 16, v228
	v_lshl_add_u64 v[38:39], v[32:33], 0, s[4:5]
	s_mov_b64 s[4:5], 0x1c00
	s_ashr_i32 s7, s6, 31
	v_cmp_lt_i32_e32 vcc, v3, v2
	v_lshl_add_u64 v[40:41], v[32:33], 0, s[4:5]
	s_lshl_b64 s[4:5], s[6:7], 13
	v_readlane_b32 s8, v255, 1
	v_cndmask_b32_e32 v3, v228, v3, vcc
	v_readlane_b32 s9, v255, 2
	s_add_u32 s8, s8, s4
	v_lshlrev_b32_e32 v110, 2, v3
	v_xor_b32_e32 v3, 32, v228
	v_readlane_b32 s13, v255, 4
	s_addc_u32 s9, s9, s5
	s_lshl_b32 s7, s10, 1
	v_readlane_b32 s10, v254, 42
	v_cmp_lt_i32_e32 vcc, v3, v2
	s_add_i32 s10, s10, s7
	v_readlane_b32 s12, v250, 6
	v_cndmask_b32_e32 v2, v228, v3, vcc
	v_readlane_b32 s13, v250, 7
	s_add_u32 s12, s12, s4
	v_lshlrev_b32_e32 v111, 2, v2
	s_addc_u32 s13, s13, s5
	s_mov_b32 s7, s6
	global_load_dwordx4 v[124:127], v[32:33], off
	global_load_dwordx4 v[128:131], v[32:33], off offset:1024
	global_load_dwordx4 v[132:135], v[32:33], off offset:2048
	global_load_dwordx4 v[136:139], v[32:33], off offset:3072
	global_load_dwordx4 v[140:143], v[34:35], off
	global_load_dwordx4 v[144:147], v[36:37], off
	global_load_dwordx4 v[148:151], v[38:39], off
	global_load_dwordx4 v[152:155], v[40:41], off
.LBB0_1349:
	s_ashr_i32 s11, s10, 31
	s_lshl_b64 s[4:5], s[10:11], 2
	s_add_u32 s14, s18, s4
	s_addc_u32 s15, s19, s5
	global_load_dwordx2 v[2:3], v187, s[14:15]
	s_add_i32 s14, s10, 1
	s_ashr_i32 s15, s14, 31
	s_add_u32 s4, s23, s4
	s_addc_u32 s5, s17, s5
	global_load_dword v52, v187, s[4:5]
	s_lshl_b64 s[4:5], s[14:15], 2
	s_add_u32 s4, s23, s4
	s_addc_u32 s5, s17, s5
	global_load_dword v53, v187, s[4:5]
	v_lshl_add_u64 v[4:5], s[12:13], 0, v[186:187]
	s_mov_b32 s4, 0x36da1000
	s_add_i32 s7, s7, s16
	s_waitcnt vmcnt(0)
	v_ashrrev_i32_e32 v7, 31, v2
	v_mov_b32_e32 v6, v2
	v_lshlrev_b64 v[6:7], 12, v[6:7]
	v_lshl_add_u64 v[18:19], v[28:29], 0, v[6:7]
	v_lshl_add_u64 v[76:77], v[30:31], 0, v[6:7]
	v_add_co_u32_e32 v6, vcc, s4, v4
	v_ashrrev_i32_e32 v9, 31, v3
	s_nop 0
	v_addc_co_u32_e32 v7, vcc, 0, v5, vcc
	v_mov_b32_e32 v8, v3
	v_add_co_u32_e32 v96, vcc, s28, v4
	v_lshlrev_b64 v[2:3], 12, v[8:9]
	s_nop 0
	v_addc_co_u32_e32 v97, vcc, 0, v5, vcc
	v_lshl_add_u64 v[68:69], v[28:29], 0, v[2:3]
	v_lshl_add_u64 v[92:93], v[30:31], 0, v[2:3]
	global_load_dwordx2 v[104:105], v[18:19], off
	global_load_dwordx2 v[100:101], v[68:69], off
	global_load_dwordx2 v[106:107], v[76:77], off
	global_load_dwordx2 v[102:103], v[92:93], off
	global_load_dwordx4 v[24:27], v[96:97], off offset:-4096
	global_load_dwordx2 v[2:3], v[18:19], off offset:512
	global_load_dwordx2 v[4:5], v[68:69], off offset:512
	global_load_dwordx2 v[8:9], v[76:77], off offset:512
	global_load_dwordx2 v[14:15], v[92:93], off offset:512
	global_load_dwordx4 v[10:13], v[6:7], off offset:1024
	v_mov_b32_e32 v94, v53
	s_waitcnt vmcnt(4)
	v_lshlrev_b32_e32 v16, 16, v2
	s_waitcnt vmcnt(3)
	v_lshlrev_b32_e32 v17, 16, v4
	s_waitcnt vmcnt(2)
	v_lshlrev_b32_e32 v20, 16, v8
	s_waitcnt vmcnt(1)
	v_lshlrev_b32_e32 v21, 16, v14
	v_pk_add_f32 v[16:17], v[16:17], v[20:21]
	v_and_b32_e32 v21, 0xffff0000, v14
	v_pk_mul_f32 v[64:65], v[52:53], v[16:17]
	v_and_b32_e32 v17, 0xffff0000, v4
	v_and_b32_e32 v16, 0xffff0000, v2
	v_and_b32_e32 v20, 0xffff0000, v8
	v_pk_add_f32 v[16:17], v[16:17], v[20:21]
	v_lshlrev_b32_e32 v21, 16, v15
	v_pk_mul_f32 v[66:67], v[52:53], v[16:17]
	v_lshlrev_b32_e32 v17, 16, v5
	v_lshlrev_b32_e32 v16, 16, v3
	v_lshlrev_b32_e32 v20, 16, v9
	v_and_b32_e32 v5, 0xffff0000, v5
	v_and_b32_e32 v4, 0xffff0000, v3
	v_and_b32_e32 v3, 0xffff0000, v15
	v_and_b32_e32 v2, 0xffff0000, v9
	v_pk_add_f32 v[16:17], v[16:17], v[20:21]
	v_pk_add_f32 v[2:3], v[4:5], v[2:3]
	v_pk_mul_f32 v[54:55], v[52:53], v[16:17]
	v_pk_mul_f32 v[56:57], v[52:53], v[2:3]
	global_load_dwordx2 v[8:9], v[18:19], off offset:1024
	global_load_dwordx2 v[14:15], v[68:69], off offset:1024
	global_load_dwordx2 v[16:17], v[76:77], off offset:1024
	global_load_dwordx2 v[20:21], v[92:93], off offset:1024
	global_load_dwordx4 v[2:5], v[6:7], off offset:2048
	v_lshlrev_b32_e32 v120, 16, v102
	v_and_b32_e32 v121, 0xffff0000, v102
	v_lshlrev_b32_e32 v102, 16, v103
	v_and_b32_e32 v103, 0xffff0000, v103
	s_waitcnt vmcnt(4)
; __global__ void __launch_bounds__(NWAVES * 64, 2) trunk_fwd(Args args) {
;     ...
;                     for (int jj = 0; jj < 8; ++jj) { const v2u a = y0[64 * jj], c = y1[64 * jj], a2 = z0[64 * jj], c2 = z1[64 * jj]; f32x4 x = xr[64 * jj];
;                         x.x += g0 * (bflo(a.x) + bflo(a2.x)) + g1 * (bflo(c.x) + bflo(c2.x)); x.y += g0 * (bfhi(a.x) + bfhi(a2.x)) + g1 * (bfhi(c.x) + bfhi(c2.x));
;                         x.z += g0 * (bflo(a.y) + bflo(a2.y)) + g1 * (bflo(c.y) + bflo(c2.y)); x.w += g0 * (bfhi(a.y) + bfhi(a2.y)) + g1 * (bfhi(c.y) + bfhi(c2.y));
;                         v[jj] = x; s += (x.x * x.x + x.y * x.y) + (x.z * x.z + x.w * x.w); }
	v_lshlrev_b32_e32 v23, 16, v9
	v_lshlrev_b32_e32 v22, 16, v8
	s_waitcnt vmcnt(2)
	v_lshlrev_b32_e32 v43, 16, v17
	v_lshlrev_b32_e32 v42, 16, v16
	v_and_b32_e32 v9, 0xffff0000, v9
	v_and_b32_e32 v8, 0xffff0000, v8
	v_and_b32_e32 v17, 0xffff0000, v17
	v_and_b32_e32 v16, 0xffff0000, v16
	v_pk_add_f32 v[22:23], v[22:23], v[42:43]
	v_lshlrev_b32_e32 v43, 16, v15
	v_lshlrev_b32_e32 v42, 16, v14
	s_waitcnt vmcnt(1)
	v_lshlrev_b32_e32 v45, 16, v21
	v_lshlrev_b32_e32 v44, 16, v20
	v_pk_add_f32 v[8:9], v[8:9], v[16:17]
	v_and_b32_e32 v15, 0xffff0000, v15
	v_and_b32_e32 v14, 0xffff0000, v14
	v_and_b32_e32 v17, 0xffff0000, v21
	v_and_b32_e32 v16, 0xffff0000, v20
	v_pk_add_f32 v[42:43], v[42:43], v[44:45]
	v_pk_add_f32 v[14:15], v[14:15], v[16:17]
	v_pk_mul_f32 v[42:43], v[94:95], v[42:43] op_sel_hi:[0,1]
	v_pk_mul_f32 v[14:15], v[94:95], v[14:15] op_sel_hi:[0,1]
	v_pk_fma_f32 v[22:23], v[52:53], v[22:23], v[42:43] op_sel_hi:[0,1,1]
	s_waitcnt vmcnt(0)
	v_mov_b32_e32 v42, v2
	v_mov_b32_e32 v43, v4
	v_pk_fma_f32 v[8:9], v[52:53], v[8:9], v[14:15] op_sel_hi:[0,1,1]
	v_mov_b32_e32 v4, v3
	v_pk_add_f32 v[58:59], v[42:43], v[22:23]
	v_pk_add_f32 v[42:43], v[4:5], v[8:9]
	s_nop 0
	v_pk_mul_f32 v[2:3], v[42:43], v[42:43]
	s_nop 0
	v_pk_fma_f32 v[2:3], v[58:59], v[58:59], v[2:3]
	s_nop 0
	v_pk_add_f32 v[62:63], v[2:3], v[2:3] op_sel:[0,1] op_sel_hi:[1,0]
	global_load_dwordx2 v[8:9], v[18:19], off offset:1536
	global_load_dwordx2 v[14:15], v[68:69], off offset:1536
	global_load_dwordx2 v[16:17], v[76:77], off offset:1536
	global_load_dwordx2 v[20:21], v[92:93], off offset:1536
	global_load_dwordx4 v[2:5], v[6:7], off offset:3072
	s_waitcnt vmcnt(4)
	v_lshlrev_b32_e32 v6, 16, v8
	v_and_b32_e32 v7, 0xffff0000, v8
	s_waitcnt vmcnt(2)
	v_lshlrev_b32_e32 v22, 16, v16
	v_and_b32_e32 v23, 0xffff0000, v16
	v_pk_add_f32 v[6:7], v[6:7], v[22:23]
	v_lshlrev_b32_e32 v22, 16, v14
	v_and_b32_e32 v23, 0xffff0000, v14
	s_waitcnt vmcnt(1)
	v_lshlrev_b32_e32 v44, 16, v20
	v_and_b32_e32 v45, 0xffff0000, v20
	v_pk_add_f32 v[22:23], v[22:23], v[44:45]
	v_lshlrev_b32_e32 v8, 16, v21
	v_pk_mul_f32 v[22:23], v[94:95], v[22:23] op_sel_hi:[0,1]
	v_pk_fma_f32 v[6:7], v[52:53], v[6:7], v[22:23] op_sel_hi:[0,1,1]
	s_waitcnt vmcnt(0)
	v_pk_add_f32 v[44:45], v[2:3], v[6:7]
	v_lshlrev_b32_e32 v6, 16, v17
	v_mul_f32_e32 v2, v45, v45
	v_pk_fma_f32 v[82:83], v[44:45], v[44:45], v[2:3] op_sel_hi:[1,1,0]
	v_lshlrev_b32_e32 v2, 16, v9
	v_and_b32_e32 v3, 0xffff0000, v9
	v_and_b32_e32 v7, 0xffff0000, v17
	v_pk_add_f32 v[2:3], v[2:3], v[6:7]
	v_lshlrev_b32_e32 v6, 16, v15
	v_and_b32_e32 v7, 0xffff0000, v15
	v_and_b32_e32 v9, 0xffff0000, v21
	v_pk_add_f32 v[6:7], v[6:7], v[8:9]
	s_nop 0
	v_pk_mul_f32 v[6:7], v[94:95], v[6:7] op_sel_hi:[0,1]
	v_pk_fma_f32 v[2:3], v[52:53], v[2:3], v[6:7] op_sel_hi:[0,1,1]
	v_pk_add_f32 v[46:47], v[4:5], v[2:3]
	s_nop 0
	v_mul_f32_e32 v2, v47, v47
	v_pk_fma_f32 v[86:87], v[46:47], v[46:47], v[2:3] op_sel_hi:[1,1,0]
	global_load_dwordx2 v[2:3], v[18:19], off offset:2048
	global_load_dwordx2 v[4:5], v[68:69], off offset:2048
	global_load_dwordx2 v[6:7], v[76:77], off offset:2048
	global_load_dwordx2 v[8:9], v[92:93], off offset:2048
	global_load_dwordx4 v[20:23], v[96:97], off
	s_waitcnt vmcnt(4)
	v_lshlrev_b32_e32 v14, 16, v3
	s_waitcnt vmcnt(3)
	v_lshlrev_b32_e32 v15, 16, v5
	s_waitcnt vmcnt(2)
	v_lshlrev_b32_e32 v16, 16, v7
	s_waitcnt vmcnt(1)
	v_lshlrev_b32_e32 v17, 16, v9
	v_pk_add_f32 v[78:79], v[14:15], v[16:17]
	v_and_b32_e32 v15, 0xffff0000, v5
	v_and_b32_e32 v14, 0xffff0000, v3
	v_and_b32_e32 v17, 0xffff0000, v9
	v_and_b32_e32 v16, 0xffff0000, v7
	v_pk_add_f32 v[88:89], v[14:15], v[16:17]
	v_lshlrev_b32_e32 v14, 16, v2
	v_and_b32_e32 v15, 0xffff0000, v2
	v_lshlrev_b32_e32 v2, 16, v6
	v_and_b32_e32 v3, 0xffff0000, v6
	v_lshlrev_b32_e32 v6, 16, v4
	v_and_b32_e32 v7, 0xffff0000, v4
	v_lshlrev_b32_e32 v4, 16, v8
	v_and_b32_e32 v5, 0xffff0000, v8
	v_pk_add_f32 v[4:5], v[6:7], v[4:5]
	v_pk_add_f32 v[2:3], v[14:15], v[2:3]
	v_pk_mul_f32 v[4:5], v[94:95], v[4:5] op_sel_hi:[0,1]
	v_pk_fma_f32 v[2:3], v[52:53], v[2:3], v[4:5] op_sel_hi:[0,1,1]
	s_waitcnt vmcnt(0)
	v_pk_add_f32 v[48:49], v[20:21], v[2:3]
	s_nop 0
	v_mul_f32_e32 v2, v49, v49
	v_pk_fma_f32 v[90:91], v[48:49], v[48:49], v[2:3] op_sel_hi:[1,1,0]
	global_load_dwordx2 v[2:3], v[18:19], off offset:2560
	global_load_dwordx2 v[4:5], v[68:69], off offset:2560
	global_load_dwordx2 v[14:15], v[76:77], off offset:2560
	global_load_dwordx2 v[16:17], v[92:93], off offset:2560
	global_load_dwordx4 v[6:9], v[96:97], off offset:1024
	s_waitcnt vmcnt(4)
	v_lshlrev_b32_e32 v20, 16, v2
	s_waitcnt vmcnt(3)
	v_lshlrev_b32_e32 v21, 16, v4
	s_waitcnt vmcnt(2)
	v_lshlrev_b32_e32 v50, 16, v14
	s_waitcnt vmcnt(1)
	v_lshlrev_b32_e32 v51, 16, v16
	v_pk_add_f32 v[20:21], v[20:21], v[50:51]
	v_and_b32_e32 v14, 0xffff0000, v14
	v_pk_mul_f32 v[20:21], v[52:53], v[20:21]
	v_and_b32_e32 v2, 0xffff0000, v2
	v_add_f32_e32 v20, v20, v21
	v_add_f32_e32 v2, v14, v2
	s_waitcnt vmcnt(0)
	v_add_f32_e32 v6, v6, v20
	v_mul_f32_e32 v20, v52, v2
	v_and_b32_e32 v2, 0xffff0000, v16
	v_and_b32_e32 v4, 0xffff0000, v4
	v_add_f32_e32 v2, v2, v4
	v_mul_f32_e32 v114, v53, v2
	v_lshlrev_b32_e32 v51, 16, v5
	v_lshlrev_b32_e32 v50, 16, v3
	v_lshlrev_b32_e32 v61, 16, v17
	v_lshlrev_b32_e32 v60, 16, v15
	v_and_b32_e32 v5, 0xffff0000, v5
	v_and_b32_e32 v4, 0xffff0000, v3
	v_and_b32_e32 v3, 0xffff0000, v17
	v_and_b32_e32 v2, 0xffff0000, v15
	v_pk_add_f32 v[50:51], v[50:51], v[60:61]
	v_pk_add_f32 v[2:3], v[4:5], v[2:3]
	v_pk_mul_f32 v[60:61], v[52:53], v[50:51]
	v_pk_mul_f32 v[50:51], v[52:53], v[2:3]
	global_load_dwordx2 v[2:3], v[18:19], off offset:3072
	global_load_dwordx2 v[4:5], v[68:69], off offset:3072
	global_load_dwordx2 v[98:99], v[76:77], off offset:3072
	global_load_dwordx2 v[112:113], v[92:93], off offset:3072
	global_load_dwordx4 v[14:17], v[96:97], off offset:2048
	v_mul_f32_e32 v80, v6, v6
	s_waitcnt vmcnt(4)
; __global__ void __launch_bounds__(NWAVES * 64, 2) trunk_fwd(Args args) {
;     ...
;                     for (int jj = 0; jj < 8; ++jj) { const v2u a = y0[64 * jj], c = y1[64 * jj], a2 = z0[64 * jj], c2 = z1[64 * jj]; f32x4 x = xr[64 * jj];
;                         x.x += g0 * (bflo(a.x) + bflo(a2.x)) + g1 * (bflo(c.x) + bflo(c2.x)); x.y += g0 * (bfhi(a.x) + bfhi(a2.x)) + g1 * (bfhi(c.x) + bfhi(c2.x));
;                         x.z += g0 * (bflo(a.y) + bflo(a2.y)) + g1 * (bflo(c.y) + bflo(c2.y)); x.w += g0 * (bfhi(a.y) + bfhi(a2.y)) + g1 * (bfhi(c.y) + bfhi(c2.y));
;                         v[jj] = x; s += (x.x * x.x + x.y * x.y) + (x.z * x.z + x.w * x.w); }
	v_lshlrev_b32_e32 v70, 16, v2
	s_waitcnt vmcnt(3)
	v_lshlrev_b32_e32 v71, 16, v4
	s_waitcnt vmcnt(2)
	v_lshlrev_b32_e32 v84, 16, v98
	s_waitcnt vmcnt(1)
	v_lshlrev_b32_e32 v85, 16, v112
	v_pk_add_f32 v[84:85], v[70:71], v[84:85]
	v_and_b32_e32 v71, 0xffff0000, v4
	v_and_b32_e32 v70, 0xffff0000, v2
	v_and_b32_e32 v117, 0xffff0000, v112
	v_and_b32_e32 v116, 0xffff0000, v98
	v_pk_add_f32 v[70:71], v[70:71], v[116:117]
	v_and_b32_e32 v4, 0xffff0000, v3
	v_pk_mul_f32 v[70:71], v[52:53], v[70:71]
	v_lshlrev_b32_e32 v117, 16, v113
	v_add_f32_e32 v2, v70, v71
	s_waitcnt vmcnt(0)
	v_add_f32_e32 v112, v15, v2
	v_lshlrev_b32_e32 v71, 16, v5
	v_lshlrev_b32_e32 v70, 16, v3
	v_and_b32_e32 v5, 0xffff0000, v5
	v_and_b32_e32 v3, 0xffff0000, v113
	v_and_b32_e32 v2, 0xffff0000, v99
	v_pk_add_f32 v[2:3], v[4:5], v[2:3]
	v_lshlrev_b32_e32 v116, 16, v99
	v_pk_mul_f32 v[2:3], v[52:53], v[2:3]
	v_pk_add_f32 v[70:71], v[70:71], v[116:117]
	v_add_f32_e32 v2, v2, v3
	v_add_f32_e32 v113, v17, v2
	global_load_dwordx2 v[18:19], v[18:19], off offset:3584
	s_nop 0
	global_load_dwordx2 v[116:117], v[68:69], off offset:3584
	s_nop 0
	global_load_dwordx2 v[76:77], v[76:77], off offset:3584
	s_nop 0
	global_load_dwordx2 v[118:119], v[92:93], off offset:3584
	global_load_dwordx4 v[2:5], v[96:97], off offset:3072
	v_mov_b32_e32 v92, v7
	v_mov_b32_e32 v98, v22
	v_mul_f32_e32 v22, v53, v79
	v_pk_fma_f32 v[78:79], v[52:53], v[78:79], v[22:23] op_sel_hi:[1,1,0]
	v_mul_f32_e32 v22, v53, v89
	v_mov_b32_e32 v93, v52
	v_mul_f32_e32 v74, v112, v112
	v_mul_f32_e32 v72, v113, v113
	s_waitcnt vmcnt(4)
	v_and_b32_e32 v21, 0xffff0000, v18
	s_waitcnt vmcnt(3)
	v_and_b32_e32 v15, 0xffff0000, v116
	s_waitcnt vmcnt(2)
	v_and_b32_e32 v115, 0xffff0000, v76
	s_waitcnt vmcnt(1)
	v_and_b32_e32 v7, 0xffff0000, v118
	v_add_f32_e32 v7, v7, v15
	v_mul_f32_e32 v97, v53, v7
	v_lshlrev_b32_e32 v7, 16, v19
	v_lshlrev_b32_e32 v15, 16, v77
	v_add_f32_e32 v7, v15, v7
	v_mul_f32_e32 v15, v52, v7
	v_lshlrev_b32_e32 v7, 16, v117
	v_lshlrev_b32_e32 v17, 16, v119
	v_add_f32_e32 v7, v17, v7
	v_pk_add_f32 v[20:21], v[20:21], v[114:115]
	v_mul_f32_e32 v114, v53, v7
	v_and_b32_e32 v7, 0xffff0000, v77
	v_and_b32_e32 v17, 0xffff0000, v19
	v_add_f32_e32 v7, v7, v17
	v_lshlrev_b32_e32 v99, 16, v18
	v_lshlrev_b32_e32 v95, 16, v116
	v_lshlrev_b32_e32 v81, 16, v118
	v_mul_f32_e32 v17, v52, v7
	v_and_b32_e32 v7, 0xffff0000, v119
	v_and_b32_e32 v18, 0xffff0000, v117
	v_lshlrev_b32_e32 v116, 16, v104
	v_and_b32_e32 v117, 0xffff0000, v104
	v_lshlrev_b32_e32 v118, 16, v106
	v_and_b32_e32 v119, 0xffff0000, v106
	v_pk_add_f32 v[116:117], v[116:117], v[118:119]
	v_lshlrev_b32_e32 v118, 16, v100
	v_and_b32_e32 v119, 0xffff0000, v100
	v_lshlrev_b32_e32 v100, 16, v101
	v_and_b32_e32 v101, 0xffff0000, v101
	v_pk_add_f32 v[118:119], v[118:119], v[120:121]
	v_pk_add_f32 v[100:101], v[100:101], v[102:103]
	v_lshlrev_b32_e32 v83, 16, v76
	v_pk_mul_f32 v[118:119], v[94:95], v[118:119] op_sel_hi:[0,1]
	v_pk_mul_f32 v[100:101], v[94:95], v[100:101] op_sel_hi:[0,1]
	v_mov_b32_e32 v94, v23
	v_pk_fma_f32 v[22:23], v[52:53], v[88:89], v[22:23] op_sel_hi:[1,1,0]
	v_lshlrev_b32_e32 v104, 16, v105
	v_and_b32_e32 v105, 0xffff0000, v105
	v_lshlrev_b32_e32 v106, 16, v107
	v_and_b32_e32 v107, 0xffff0000, v107
	v_mov_b32_e32 v79, v83
	v_mov_b32_e32 v23, v81
	v_pk_add_f32 v[104:105], v[104:105], v[106:107]
	v_pk_add_f32 v[78:79], v[98:99], v[78:79]
	v_pk_add_f32 v[88:89], v[94:95], v[22:23]
	v_pk_fma_f32 v[100:101], v[52:53], v[104:105], v[100:101] op_sel_hi:[0,1,1]
	v_mov_b32_e32 v98, v78
	v_mov_b32_e32 v99, v52
	v_mov_b32_e32 v22, v88
	v_mov_b32_e32 v23, v53
	v_pk_add_f32 v[68:69], v[92:93], v[20:21]
	v_pk_mul_f32 v[92:93], v[92:93], v[20:21]
	v_pk_add_f32 v[26:27], v[26:27], v[100:101]
	v_pk_mul_f32 v[100:101], v[98:99], v[78:79]
	v_pk_mul_f32 v[22:23], v[22:23], v[88:89]
	v_mov_b32_e32 v92, v68
	v_mov_b32_e32 v83, v101
	v_mov_b32_e32 v87, v23
	v_pk_fma_f32 v[22:23], v[98:99], v[78:79], v[22:23]
	s_waitcnt vmcnt(0)
; __global__ void __launch_bounds__(NWAVES * 64, 2) trunk_fwd(Args args) {
;     ...
;                         v[jj] = x; s += (x.x * x.x + x.y * x.y) + (x.z * x.z + x.w * x.w); }
;                     const float rstd = 1.0f / sqrtf(wave_sum(s) * (1.0f / D) + EPS);
;                     const f32x4* gr = (const f32x4*)args.in[I_NF] + lane; f32x4* orow = (f32x4*)(args.out + (size_t)m * D) + lane;
; #pragma unroll
;                     for (int jj = 0; jj < 8; ++jj) { const f32x4 gg = gr[64 * jj]; orow[64 * jj] = (f32x4){v[jj].x * rstd * gg.x, v[jj].y * rstd * gg.y, v[jj].z * rstd * gg.z, v[jj].w * rstd * gg.w}; }
	v_mov_b32_e32 v91, v2
	v_mov_b32_e32 v96, v68
	v_pk_add_f32 v[86:87], v[82:83], v[86:87]
	v_pk_add_f32 v[90:91], v[90:91], v[22:23]
	v_pk_mul_f32 v[22:23], v[68:69], v[68:69]
	v_pk_add_f32 v[82:83], v[92:93], v[96:97]
	v_mov_b32_e32 v81, v3
	v_mov_b32_e32 v23, v83
	v_pk_add_f32 v[22:23], v[80:81], v[22:23]
	v_mul_f32_e32 v80, v53, v85
	v_pk_fma_f32 v[80:81], v[52:53], v[84:85], v[80:81] op_sel_hi:[1,1,0]
	v_add_f32_e32 v7, v7, v18
	v_mov_b32_e32 v81, v114
	v_pk_add_f32 v[14:15], v[14:15], v[80:81]
	v_mov_b32_e32 v81, v4
	v_mul_f32_e32 v4, v53, v71
	v_mul_f32_e32 v7, v53, v7
	v_pk_fma_f32 v[116:117], v[52:53], v[116:117], v[118:119] op_sel_hi:[0,1,1]
	v_pk_fma_f32 v[52:53], v[52:53], v[70:71], v[4:5] op_sel_hi:[1,1,0]
	v_mov_b32_e32 v80, v14
	v_mov_b32_e32 v53, v7
	v_pk_add_f32 v[16:17], v[16:17], v[52:53]
	v_pk_add_f32 v[80:81], v[80:81], v[14:15]
	v_mov_b32_e32 v4, v16
	v_pk_add_f32 v[4:5], v[4:5], v[16:17]
	v_pk_fma_f32 v[52:53], v[14:15], v[14:15], v[74:75]
	v_pk_mul_f32 v[70:71], v[80:81], v[80:81]
	v_pk_mul_f32 v[84:85], v[4:5], v[4:5]
	v_mov_b32_e32 v53, v71
	v_pk_fma_f32 v[70:71], v[16:17], v[16:17], v[72:73]
	v_pk_add_f32 v[24:25], v[24:25], v[116:117]
	v_mov_b32_e32 v71, v85
	v_pk_add_f32 v[70:71], v[52:53], v[70:71]
	v_mov_b32_e32 v52, v64
	v_mov_b32_e32 v53, v66
	v_mov_b32_e32 v66, v65
	v_pk_add_f32 v[52:53], v[52:53], v[66:67]
	v_mov_b32_e32 v64, v25
	v_pk_add_f32 v[52:53], v[10:11], v[52:53]
	v_mov_b32_e32 v10, v24
	v_mov_b32_e32 v65, v53
	v_mov_b32_e32 v11, v52
	v_pk_mul_f32 v[64:65], v[64:65], v[64:65]
	v_pk_fma_f32 v[10:11], v[10:11], v[10:11], v[64:65]
	v_mov_b32_e32 v64, v54
	v_mov_b32_e32 v65, v56
	v_mov_b32_e32 v56, v55
	v_pk_add_f32 v[54:55], v[64:65], v[56:57]
	v_mov_b32_e32 v56, v27
	v_pk_add_f32 v[54:55], v[12:13], v[54:55]
	v_mov_b32_e32 v12, v26
	v_mov_b32_e32 v57, v55
	v_mov_b32_e32 v13, v54
	v_pk_mul_f32 v[56:57], v[56:57], v[56:57]
	v_lshl_add_u64 v[76:77], s[8:9], 0, v[186:187]
	v_pk_fma_f32 v[12:13], v[12:13], v[12:13], v[56:57]
	v_mov_b32_e32 v79, v88
	v_pk_add_f32 v[10:11], v[10:11], v[12:13]
	v_mov_b32_e32 v7, v68
	v_pk_add_f32 v[10:11], v[10:11], v[10:11] op_sel:[0,1] op_sel_hi:[1,0]
	s_add_u32 s8, s8, s38
	v_pk_add_f32 v[10:11], v[10:11], v[62:63]
	s_addc_u32 s9, s9, s39
	v_mov_b32_e32 v11, v2
	v_pk_add_f32 v[10:11], v[10:11], v[86:87]
	s_add_i32 s10, s10, s21
	v_pk_add_f32 v[56:57], v[10:11], v[90:91]
	v_pk_mul_f32 v[12:13], v[10:11], v[90:91]
	s_add_u32 s12, s12, s38
	v_mov_b32_e32 v57, v13
	v_mov_b32_e32 v12, v58
	v_mov_b32_e32 v13, v42
	v_mov_b32_e32 v42, v59
	v_mov_b32_e32 v58, v60
	v_mov_b32_e32 v59, v50
	v_mov_b32_e32 v50, v61
	v_pk_add_f32 v[50:51], v[58:59], v[50:51]
	s_addc_u32 s13, s13, s39
	v_pk_add_f32 v[8:9], v[8:9], v[50:51]
	s_cmpk_lt_i32 s7, 0x2000
	v_pk_mul_f32 v[50:51], v[8:9], v[8:9]
	s_nop 0
	v_mov_b32_e32 v2, v50
	v_mov_b32_e32 v82, v51
	v_pk_add_f32 v[2:3], v[2:3], v[82:83]
	s_nop 0
	v_pk_add_f32 v[50:51], v[22:23], v[2:3]
	v_pk_mul_f32 v[2:3], v[22:23], v[2:3]
	v_mov_b32_e32 v22, v11
	v_mov_b32_e32 v51, v3
	v_pk_add_f32 v[2:3], v[56:57], v[50:51]
	s_nop 0
	v_pk_add_f32 v[2:3], v[2:3], v[70:71]
	s_nop 0
	v_add_f32_e32 v2, v2, v3
	ds_bpermute_b32 v3, v73, v2
	s_waitcnt lgkmcnt(0)
	v_add_f32_e32 v2, v2, v3
	ds_bpermute_b32 v3, v75, v2
	s_waitcnt lgkmcnt(0)
	v_add_f32_e32 v2, v2, v3
	ds_bpermute_b32 v3, v108, v2
	s_waitcnt lgkmcnt(0)
	v_add_f32_e32 v2, v2, v3
	ds_bpermute_b32 v3, v109, v2
	s_waitcnt lgkmcnt(0)
	v_add_f32_e32 v2, v2, v3
	ds_bpermute_b32 v3, v110, v2
	s_waitcnt lgkmcnt(0)
	v_add_f32_e32 v2, v2, v3
	ds_bpermute_b32 v3, v111, v2
	s_waitcnt lgkmcnt(0)
	v_add_f32_e32 v2, v2, v3
	v_fmamk_f32 v2, v2, 0x3a000000, v226
	v_cmp_gt_f32_e32 vcc, s22, v2
	v_mul_f32_e32 v3, 0x4f800000, v2
	s_nop 0
	v_cndmask_b32_e32 v2, v2, v3, vcc
	v_sqrt_f32_e32 v3, v2
	s_nop 0
	v_add_u32_e32 v4, -1, v3
	v_fma_f32 v10, -v4, v3, v2
	v_cmp_ge_f32_e64 s[4:5], 0, v10
	v_add_u32_e32 v10, 1, v3
	s_nop 0
	v_cndmask_b32_e64 v4, v3, v4, s[4:5]
	v_fma_f32 v3, -v10, v3, v2
	v_cmp_lt_f32_e64 s[4:5], 0, v3
	s_nop 1
	v_cndmask_b32_e64 v3, v4, v10, s[4:5]
	v_mul_f32_e32 v4, 0x37800000, v3
	v_cndmask_b32_e32 v3, v3, v4, vcc
	v_cmp_class_f32_e32 vcc, v2, v225
	s_nop 1
	v_cndmask_b32_e32 v2, v3, v2, vcc
	v_div_scale_f32 v3, s[4:5], v2, v2, 1.0
	v_rcp_f32_e32 v4, v3
	s_nop 0
	v_fma_f32 v10, -v3, v4, 1.0
	v_fmac_f32_e32 v4, v10, v4
	v_div_scale_f32 v10, vcc, 1.0, v2, 1.0
	v_mul_f32_e32 v15, v10, v4
	v_fma_f32 v17, -v3, v15, v10
	v_fmac_f32_e32 v15, v17, v4
	v_fma_f32 v3, -v3, v15, v10
	v_div_fmas_f32 v3, v3, v4, v15
	v_div_fixup_f32 v10, v3, v2, 1.0
	v_pk_mul_f32 v[2:3], v[10:11], v[24:25] op_sel_hi:[0,1]
	v_pk_mul_f32 v[24:25], v[10:11], v[26:27] op_sel_hi:[0,1]
	v_pk_mul_f32 v[20:21], v[126:127], v[24:25]
	v_pk_mul_f32 v[18:19], v[124:125], v[2:3]
	global_store_dwordx4 v[76:77], v[18:21], off
	s_nop 1
	v_pk_mul_f32 v[2:3], v[10:11], v[54:55] op_sel_hi:[0,1]
	v_pk_mul_f32 v[24:25], v[10:11], v[52:53] op_sel_hi:[0,1]
	v_pk_mul_f32 v[6:7], v[10:11], v[6:7] op_sel_hi:[0,1]
	v_mov_b32_e32 v15, v112
	v_mov_b32_e32 v17, v113
	v_pk_mul_f32 v[14:15], v[10:11], v[14:15] op_sel_hi:[0,1]
	v_mov_b32_e32 v4, v81
	v_pk_mul_f32 v[4:5], v[10:11], v[4:5] op_sel_hi:[0,1]
	v_pk_mul_f32 v[18:19], v[128:129], v[24:25]
	v_pk_mul_f32 v[20:21], v[130:131], v[2:3]
	global_store_dwordx4 v[76:77], v[18:21], off offset:1024
	s_nop 1
	v_pk_mul_f32 v[2:3], v[10:11], v[12:13] op_sel_hi:[0,1]
	v_pk_mul_f32 v[12:13], v[10:11], v[44:45] op_sel_hi:[0,1]
	v_pk_mul_f32 v[18:19], v[132:133], v[2:3]
	v_pk_mul_f32 v[2:3], v[10:11], v[42:43] op_sel_hi:[0,1]
	v_pk_mul_f32 v[20:21], v[134:135], v[2:3]
	global_store_dwordx4 v[76:77], v[18:21], off offset:2048
	s_nop 1
	v_pk_mul_f32 v[2:3], v[10:11], v[46:47] op_sel_hi:[0,1]
	v_pk_mul_f32 v[18:19], v[136:137], v[12:13]
	v_pk_mul_f32 v[20:21], v[138:139], v[2:3]
	global_store_dwordx4 v[76:77], v[18:21], off offset:3072
	s_nop 1
	v_pk_mul_f32 v[2:3], v[10:11], v[48:49] op_sel_hi:[0,1]
	v_add_co_u32_e32 v12, vcc, s20, v76
	v_pk_mul_f32 v[18:19], v[140:141], v[2:3]
	v_pk_mul_f32 v[2:3], v[10:11], v[78:79] op_sel_hi:[0,1]
	v_pk_mul_f32 v[20:21], v[142:143], v[2:3]
	v_addc_co_u32_e32 v13, vcc, 0, v77, vcc
	global_store_dwordx4 v[12:13], v[18:21], off
	s_nop 1
	v_pk_mul_f32 v[2:3], v[10:11], v[8:9] op_sel_hi:[0,1]
	v_pk_mul_f32 v[6:7], v[144:145], v[6:7]
	v_pk_mul_f32 v[8:9], v[146:147], v[2:3]
	global_store_dwordx4 v[12:13], v[6:9], off offset:1024
	s_nop 1
	v_pk_mul_f32 v[2:3], v[10:11], v[16:17] op_sel_hi:[0,1]
	v_pk_mul_f32 v[6:7], v[148:149], v[14:15]
	v_pk_mul_f32 v[8:9], v[150:151], v[2:3]
	global_store_dwordx4 v[12:13], v[6:9], off offset:2048
	s_nop 1
	v_pk_mul_f32 v[2:3], v[10:11], v[22:23] op_sel_hi:[0,1]
	v_pk_mul_f32 v[2:3], v[152:153], v[2:3]
	v_pk_mul_f32 v[4:5], v[154:155], v[4:5]
	global_store_dwordx4 v[12:13], v[2:5], off offset:3072
	s_nop 1
	s_cbranch_scc1 .LBB0_1349
